# baseline (speedup 1.0000x reference)
.Lat_loop:
	ds_read_b128 v[112:115], v222 offset:8192
	ds_read_b128 v[128:131], v222 offset:10240
	ds_read_b128 v[116:119], v223 offset:8192
	ds_read_b128 v[132:135], v223 offset:10240
	s_mov_b32 m0, s63
	s_add_u32 s44, s44, 128
	s_addc_u32 s45, s45, 0
	global_load_lds_dwordx4 v220, s[42:43]
	s_mov_b32 m0, s60
	s_nop 0
	global_load_lds_dwordx4 v228, s[42:43]
	s_setprio 1
	v_exp_f32_e32 v80, v80
	v_exp_f32_e32 v81, v81
	v_exp_f32_e32 v82, v82
	v_exp_f32_e32 v83, v83
	v_exp_f32_e32 v84, v84
	v_exp_f32_e32 v85, v85
	v_exp_f32_e32 v86, v86
	v_exp_f32_e32 v87, v87
	v_cvt_pk_fp8_f32 v160, v80, v81
	v_cvt_pk_fp8_f32 v161, v84, v85
	v_exp_f32_e32 v88, v88
	v_exp_f32_e32 v89, v89
	v_cvt_pk_fp8_f32 v160, v82, v83 op_sel:[0,0,1]
	v_cvt_pk_fp8_f32 v161, v86, v87 op_sel:[0,0,1]
	v_exp_f32_e32 v90, v90
	v_exp_f32_e32 v91, v91
	v_exp_f32_e32 v92, v92
	v_exp_f32_e32 v93, v93
	v_exp_f32_e32 v94, v94
	v_exp_f32_e32 v95, v95
	s_waitcnt lgkmcnt(0)
	v_mfma_scale_f32_32x32x64_f8f6f4 v[112:127], v[112:119], v[152:159], v[64:79], v173, v194 op_sel_hi:[0,0,0]
	s_setprio 0
	ds_read_b128 v[80:83], v224 offset:0
	ds_read_b128 v[212:215], v224 offset:2048
	ds_read_b128 v[84:87], v225 offset:0
	ds_read_b128 v[216:219], v225 offset:2048
	v_cvt_pk_fp8_f32 v162, v88, v89
	v_cvt_pk_fp8_f32 v163, v92, v93
	v_exp_f32_e32 v96, v96
	v_exp_f32_e32 v97, v97
	v_cvt_pk_fp8_f32 v162, v90, v91 op_sel:[0,0,1]
	v_cvt_pk_fp8_f32 v163, v94, v95 op_sel:[0,0,1]
	v_exp_f32_e32 v98, v98
	v_exp_f32_e32 v99, v99
	v_exp_f32_e32 v100, v100
	v_exp_f32_e32 v101, v101
	v_exp_f32_e32 v102, v102
	v_exp_f32_e32 v103, v103
	v_mfma_scale_f32_32x32x64_f8f6f4 v[128:143], v[128:135], v[152:159], v[64:79], v173, v194 op_sel_hi:[0,0,0]
	v_cvt_pk_fp8_f32 v164, v96, v97
	v_cvt_pk_fp8_f32 v165, v100, v101
	v_exp_f32_e32 v104, v104
	v_exp_f32_e32 v105, v105
	v_cvt_pk_fp8_f32 v164, v98, v99 op_sel:[0,0,1]
	v_cvt_pk_fp8_f32 v165, v102, v103 op_sel:[0,0,1]
	v_exp_f32_e32 v106, v106
	v_exp_f32_e32 v107, v107
	v_exp_f32_e32 v108, v108
	v_exp_f32_e32 v109, v109
	v_exp_f32_e32 v110, v110
	v_exp_f32_e32 v111, v111
	v_cvt_pk_fp8_f32 v166, v104, v105
	v_cvt_pk_fp8_f32 v167, v108, v109
	v_cvt_pk_fp8_f32 v166, v106, v107 op_sel:[0,0,1]
	v_cvt_pk_fp8_f32 v167, v110, v111 op_sel:[0,0,1]
	s_setprio 2
	s_waitcnt lgkmcnt(0)
	v_mfma_scale_f32_32x32x64_f8f6f4 v[32:47], v[80:87], v[160:167], v[32:47], v194, v194 op_sel_hi:[0,0,0]
	ds_read_b128 v[80:83], v222 offset:16384
	ds_read_b128 v[96:99], v222 offset:18432
	ds_read_b128 v[84:87], v223 offset:16384
	ds_read_b128 v[100:103], v223 offset:18432
	v_max3_f32 v227, v112, v113, v114
	v_max3_f32 v227, v227, v115, v116
	v_max3_f32 v227, v227, v117, v118
	v_max3_f32 v227, v227, v119, v120
	v_max3_f32 v227, v227, v121, v122
	v_max3_f32 v227, v227, v123, v124
	v_max3_f32 v227, v227, v125, v126
	v_max3_f32 v227, v227, v127, v128
	s_mov_b32 m0, s66
	s_add_u32 s42, s42, 0x2000
	s_addc_u32 s43, s43, 0
	global_load_lds_dwordx4 v221, s[44:45]
	v_mfma_scale_f32_32x32x64_f8f6f4 v[16:31], v[212:219], v[160:167], v[16:31], v194, v194 op_sel_hi:[0,0,0]
	v_max3_f32 v226, v129, v130, v131
	v_max3_f32 v226, v226, v132, v133
	v_max3_f32 v226, v226, v134, v135
	v_max3_f32 v226, v226, v136, v137
	v_max3_f32 v226, v226, v138, v139
	v_max3_f32 v226, v226, v140, v141
	v_max3_f32 v226, v226, v142, v143
	s_mov_b32 m0, s67
	s_nop 0
	global_load_lds_dwordx4 v229, s[44:45]
	v_mfma_scale_f32_16x16x128_f8f6f4 v[48:51], v[144:151], v[160:167], v[48:51], v194, v194 op_sel_hi:[0,0,0]
	s_setprio 0
	v_max_f32_e32 v226, v227, v226
	v_cmp_lt_f32_e32 vcc, s36, v226
	s_cbranch_vccnz .Lat_rare_L1
.Lat_back_L1:
	s_setprio 1
	v_exp_f32_e32 v112, v112
	v_exp_f32_e32 v113, v113
	v_exp_f32_e32 v114, v114
	v_exp_f32_e32 v115, v115
	v_exp_f32_e32 v116, v116
	v_exp_f32_e32 v117, v117
	v_exp_f32_e32 v118, v118
	v_exp_f32_e32 v119, v119
	s_waitcnt lgkmcnt(0)
	v_mfma_scale_f32_32x32x64_f8f6f4 v[80:95], v[80:87], v[152:159], v[64:79], v173, v194 op_sel_hi:[0,0,0]
	v_cvt_pk_fp8_f32 v160, v112, v113
	v_cvt_pk_fp8_f32 v161, v116, v117
	v_exp_f32_e32 v120, v120
	v_exp_f32_e32 v121, v121
	v_cvt_pk_fp8_f32 v160, v114, v115 op_sel:[0,0,1]
	v_cvt_pk_fp8_f32 v161, v118, v119 op_sel:[0,0,1]
	v_exp_f32_e32 v122, v122
	v_exp_f32_e32 v123, v123
	v_exp_f32_e32 v124, v124
	v_exp_f32_e32 v125, v125
	v_exp_f32_e32 v126, v126
	v_exp_f32_e32 v127, v127
	s_setprio 0
	ds_read_b128 v[112:115], v224 offset:8192
	ds_read_b128 v[212:215], v224 offset:10240
	ds_read_b128 v[116:119], v225 offset:8192
	ds_read_b128 v[216:219], v225 offset:10240
	v_cvt_pk_fp8_f32 v162, v120, v121
	v_cvt_pk_fp8_f32 v163, v124, v125
	v_exp_f32_e32 v128, v128
	v_exp_f32_e32 v129, v129
	v_cvt_pk_fp8_f32 v162, v122, v123 op_sel:[0,0,1]
	v_cvt_pk_fp8_f32 v163, v126, v127 op_sel:[0,0,1]
	v_exp_f32_e32 v130, v130
	v_exp_f32_e32 v131, v131
	v_exp_f32_e32 v132, v132
	v_exp_f32_e32 v133, v133
	v_exp_f32_e32 v134, v134
	v_exp_f32_e32 v135, v135
	v_mfma_scale_f32_32x32x64_f8f6f4 v[96:111], v[96:103], v[152:159], v[64:79], v173, v194 op_sel_hi:[0,0,0]
	v_cvt_pk_fp8_f32 v164, v128, v129
	v_cvt_pk_fp8_f32 v165, v132, v133
	v_exp_f32_e32 v136, v136
	v_exp_f32_e32 v137, v137
	v_cvt_pk_fp8_f32 v164, v130, v131 op_sel:[0,0,1]
	v_cvt_pk_fp8_f32 v165, v134, v135 op_sel:[0,0,1]
	v_exp_f32_e32 v138, v138
	v_exp_f32_e32 v139, v139
	v_exp_f32_e32 v140, v140
	v_exp_f32_e32 v141, v141
	v_exp_f32_e32 v142, v142
	v_exp_f32_e32 v143, v143
	v_cvt_pk_fp8_f32 v166, v136, v137
	v_cvt_pk_fp8_f32 v167, v140, v141
	v_cvt_pk_fp8_f32 v166, v138, v139 op_sel:[0,0,1]
	v_cvt_pk_fp8_f32 v167, v142, v143 op_sel:[0,0,1]
	s_setprio 2
	s_waitcnt lgkmcnt(0)
	v_mfma_scale_f32_32x32x64_f8f6f4 v[32:47], v[112:119], v[160:167], v[32:47], v194, v194 op_sel_hi:[0,0,0]
	v_max3_f32 v227, v80, v81, v82
	v_max3_f32 v227, v227, v83, v84
	v_max3_f32 v227, v227, v85, v86
	v_max3_f32 v227, v227, v87, v88
	v_max3_f32 v227, v227, v89, v90
	v_max3_f32 v227, v227, v91, v92
	v_max3_f32 v227, v227, v93, v94
	v_max3_f32 v227, v227, v95, v96
	v_mfma_scale_f32_32x32x64_f8f6f4 v[16:31], v[212:219], v[160:167], v[16:31], v194, v194 op_sel_hi:[0,0,0]
	v_max3_f32 v226, v97, v98, v99
	v_max3_f32 v226, v226, v100, v101
	v_max3_f32 v226, v226, v102, v103
	v_max3_f32 v226, v226, v104, v105
	v_max3_f32 v226, v226, v106, v107
	v_max3_f32 v226, v226, v108, v109
	v_max3_f32 v226, v226, v110, v111
	v_mfma_scale_f32_16x16x128_f8f6f4 v[48:51], v[144:151], v[160:167], v[48:51], v194, v194 op_sel_hi:[0,0,0]
	s_setprio 0
	v_max_f32_e32 v226, v227, v226
	v_cmp_lt_f32_e32 vcc, s36, v226
	s_cbranch_vccnz .Lat_rare_L2
.Lat_back_L2:
	s_waitcnt vmcnt(0) lgkmcnt(0)
	s_barrier
	ds_read_b128 v[112:115], v222 offset:24576
	ds_read_b128 v[128:131], v222 offset:26624
	ds_read_b128 v[116:119], v223 offset:24576
	ds_read_b128 v[132:135], v223 offset:26624
	s_mov_b32 m0, s61
	s_add_u32 s44, s44, 128
	s_addc_u32 s45, s45, 0
	global_load_lds_dwordx4 v220, s[42:43]
	s_mov_b32 m0, s62
	s_nop 0
	global_load_lds_dwordx4 v228, s[42:43]
	s_setprio 1
	v_exp_f32_e32 v80, v80
	v_exp_f32_e32 v81, v81
	v_exp_f32_e32 v82, v82
	v_exp_f32_e32 v83, v83
	v_exp_f32_e32 v84, v84
	v_exp_f32_e32 v85, v85
	v_exp_f32_e32 v86, v86
	v_exp_f32_e32 v87, v87
	v_cvt_pk_fp8_f32 v160, v80, v81
	v_cvt_pk_fp8_f32 v161, v84, v85
	v_exp_f32_e32 v88, v88
	v_exp_f32_e32 v89, v89
	v_cvt_pk_fp8_f32 v160, v82, v83 op_sel:[0,0,1]
	v_cvt_pk_fp8_f32 v161, v86, v87 op_sel:[0,0,1]
	v_exp_f32_e32 v90, v90
	v_exp_f32_e32 v91, v91
	v_exp_f32_e32 v92, v92
	v_exp_f32_e32 v93, v93
	v_exp_f32_e32 v94, v94
	v_exp_f32_e32 v95, v95
	s_waitcnt lgkmcnt(0)
	v_mfma_scale_f32_32x32x64_f8f6f4 v[112:127], v[112:119], v[152:159], v[64:79], v173, v194 op_sel_hi:[0,0,0]
	s_setprio 0
	ds_read_b128 v[80:83], v224 offset:16384
	ds_read_b128 v[212:215], v224 offset:18432
	ds_read_b128 v[84:87], v225 offset:16384
	ds_read_b128 v[216:219], v225 offset:18432
	v_cvt_pk_fp8_f32 v162, v88, v89
	v_cvt_pk_fp8_f32 v163, v92, v93
	v_exp_f32_e32 v96, v96
	v_exp_f32_e32 v97, v97
	v_cvt_pk_fp8_f32 v162, v90, v91 op_sel:[0,0,1]
	v_cvt_pk_fp8_f32 v163, v94, v95 op_sel:[0,0,1]
	v_exp_f32_e32 v98, v98
	v_exp_f32_e32 v99, v99
	v_exp_f32_e32 v100, v100
	v_exp_f32_e32 v101, v101
	v_exp_f32_e32 v102, v102
	v_exp_f32_e32 v103, v103
	v_mfma_scale_f32_32x32x64_f8f6f4 v[128:143], v[128:135], v[152:159], v[64:79], v173, v194 op_sel_hi:[0,0,0]
	v_cvt_pk_fp8_f32 v164, v96, v97
	v_cvt_pk_fp8_f32 v165, v100, v101
	v_exp_f32_e32 v104, v104
	v_exp_f32_e32 v105, v105
	v_cvt_pk_fp8_f32 v164, v98, v99 op_sel:[0,0,1]
	v_cvt_pk_fp8_f32 v165, v102, v103 op_sel:[0,0,1]
	v_exp_f32_e32 v106, v106
	v_exp_f32_e32 v107, v107
	v_exp_f32_e32 v108, v108
	v_exp_f32_e32 v109, v109
	v_exp_f32_e32 v110, v110
	v_exp_f32_e32 v111, v111
	v_cvt_pk_fp8_f32 v166, v104, v105
	v_cvt_pk_fp8_f32 v167, v108, v109
	v_cvt_pk_fp8_f32 v166, v106, v107 op_sel:[0,0,1]
	v_cvt_pk_fp8_f32 v167, v110, v111 op_sel:[0,0,1]
	s_setprio 2
	s_waitcnt lgkmcnt(0)
	v_mfma_scale_f32_32x32x64_f8f6f4 v[32:47], v[80:87], v[160:167], v[32:47], v194, v194 op_sel_hi:[0,0,0]
	ds_read_b128 v[80:83], v222 offset:0
	ds_read_b128 v[96:99], v222 offset:2048
	ds_read_b128 v[84:87], v223 offset:0
	ds_read_b128 v[100:103], v223 offset:2048
	v_max3_f32 v227, v112, v113, v114
	v_max3_f32 v227, v227, v115, v116
	v_max3_f32 v227, v227, v117, v118
	v_max3_f32 v227, v227, v119, v120
	v_max3_f32 v227, v227, v121, v122
	v_max3_f32 v227, v227, v123, v124
	v_max3_f32 v227, v227, v125, v126
	v_max3_f32 v227, v227, v127, v128
	s_mov_b32 m0, s64
	s_add_u32 s42, s42, 0x2000
	s_addc_u32 s43, s43, 0
	global_load_lds_dwordx4 v221, s[44:45]
	v_mfma_scale_f32_32x32x64_f8f6f4 v[16:31], v[212:219], v[160:167], v[16:31], v194, v194 op_sel_hi:[0,0,0]
	v_max3_f32 v226, v129, v130, v131
	v_max3_f32 v226, v226, v132, v133
	v_max3_f32 v226, v226, v134, v135
	v_max3_f32 v226, v226, v136, v137
	v_max3_f32 v226, v226, v138, v139
	v_max3_f32 v226, v226, v140, v141
	v_max3_f32 v226, v226, v142, v143
	s_mov_b32 m0, s65
	s_nop 0
	global_load_lds_dwordx4 v229, s[44:45]
	v_mfma_scale_f32_16x16x128_f8f6f4 v[48:51], v[144:151], v[160:167], v[48:51], v194, v194 op_sel_hi:[0,0,0]
	s_setprio 0
	v_max_f32_e32 v226, v227, v226
	v_cmp_lt_f32_e32 vcc, s36, v226
	s_cbranch_vccnz .Lat_rare_L3
.Lat_back_L3:
	s_setprio 1
	v_exp_f32_e32 v112, v112
	v_exp_f32_e32 v113, v113
	v_exp_f32_e32 v114, v114
	v_exp_f32_e32 v115, v115
	v_exp_f32_e32 v116, v116
	v_exp_f32_e32 v117, v117
	v_exp_f32_e32 v118, v118
	v_exp_f32_e32 v119, v119
	s_waitcnt lgkmcnt(0)
	v_mfma_scale_f32_32x32x64_f8f6f4 v[80:95], v[80:87], v[152:159], v[64:79], v173, v194 op_sel_hi:[0,0,0]
	v_cvt_pk_fp8_f32 v160, v112, v113
	v_cvt_pk_fp8_f32 v161, v116, v117
	v_exp_f32_e32 v120, v120
	v_exp_f32_e32 v121, v121
	v_cvt_pk_fp8_f32 v160, v114, v115 op_sel:[0,0,1]
	v_cvt_pk_fp8_f32 v161, v118, v119 op_sel:[0,0,1]
	v_exp_f32_e32 v122, v122
	v_exp_f32_e32 v123, v123
	v_exp_f32_e32 v124, v124
	v_exp_f32_e32 v125, v125
	v_exp_f32_e32 v126, v126
	v_exp_f32_e32 v127, v127
	s_setprio 0
	ds_read_b128 v[112:115], v224 offset:24576
	ds_read_b128 v[212:215], v224 offset:26624
	ds_read_b128 v[116:119], v225 offset:24576
	ds_read_b128 v[216:219], v225 offset:26624
	v_cvt_pk_fp8_f32 v162, v120, v121
	v_cvt_pk_fp8_f32 v163, v124, v125
	v_exp_f32_e32 v128, v128
	v_exp_f32_e32 v129, v129
	v_cvt_pk_fp8_f32 v162, v122, v123 op_sel:[0,0,1]
	v_cvt_pk_fp8_f32 v163, v126, v127 op_sel:[0,0,1]
	v_exp_f32_e32 v130, v130
	v_exp_f32_e32 v131, v131
	v_exp_f32_e32 v132, v132
	v_exp_f32_e32 v133, v133
	v_exp_f32_e32 v134, v134
	v_exp_f32_e32 v135, v135
	v_mfma_scale_f32_32x32x64_f8f6f4 v[96:111], v[96:103], v[152:159], v[64:79], v173, v194 op_sel_hi:[0,0,0]
	v_cvt_pk_fp8_f32 v164, v128, v129
	v_cvt_pk_fp8_f32 v165, v132, v133
	v_exp_f32_e32 v136, v136
	v_exp_f32_e32 v137, v137
	v_cvt_pk_fp8_f32 v164, v130, v131 op_sel:[0,0,1]
	v_cvt_pk_fp8_f32 v165, v134, v135 op_sel:[0,0,1]
	v_exp_f32_e32 v138, v138
	v_exp_f32_e32 v139, v139
	v_exp_f32_e32 v140, v140
	v_exp_f32_e32 v141, v141
	v_exp_f32_e32 v142, v142
	v_exp_f32_e32 v143, v143
	v_cvt_pk_fp8_f32 v166, v136, v137
	v_cvt_pk_fp8_f32 v167, v140, v141
	v_cvt_pk_fp8_f32 v166, v138, v139 op_sel:[0,0,1]
	v_cvt_pk_fp8_f32 v167, v142, v143 op_sel:[0,0,1]
	s_setprio 2
	s_waitcnt lgkmcnt(0)
	v_mfma_scale_f32_32x32x64_f8f6f4 v[32:47], v[112:119], v[160:167], v[32:47], v194, v194 op_sel_hi:[0,0,0]
	v_max3_f32 v227, v80, v81, v82
	v_max3_f32 v227, v227, v83, v84
	v_max3_f32 v227, v227, v85, v86
	v_max3_f32 v227, v227, v87, v88
	v_max3_f32 v227, v227, v89, v90
	v_max3_f32 v227, v227, v91, v92
	v_max3_f32 v227, v227, v93, v94
	v_max3_f32 v227, v227, v95, v96
	v_mfma_scale_f32_32x32x64_f8f6f4 v[16:31], v[212:219], v[160:167], v[16:31], v194, v194 op_sel_hi:[0,0,0]
	v_max3_f32 v226, v97, v98, v99
	v_max3_f32 v226, v226, v100, v101
	v_max3_f32 v226, v226, v102, v103
	v_max3_f32 v226, v226, v104, v105
	v_max3_f32 v226, v226, v106, v107
	v_max3_f32 v226, v226, v108, v109
	v_max3_f32 v226, v226, v110, v111
	v_mfma_scale_f32_16x16x128_f8f6f4 v[48:51], v[144:151], v[160:167], v[48:51], v194, v194 op_sel_hi:[0,0,0]
	s_setprio 0
	v_max_f32_e32 v226, v227, v226
	v_cmp_lt_f32_e32 vcc, s36, v226
	s_cbranch_vccnz .Lat_rare_L4
.Lat_back_L4:
	s_waitcnt vmcnt(0) lgkmcnt(0)
	s_barrier
	s_add_u32 s39, s39, 1
	s_cmp_lt_u32 s39, 3
	s_cbranch_scc1 .Lat_loop
	ds_read_b128 v[112:115], v222 offset:8192
	ds_read_b128 v[128:131], v222 offset:10240
	ds_read_b128 v[116:119], v223 offset:8192
	ds_read_b128 v[132:135], v223 offset:10240
	s_mov_b32 m0, s63
	s_add_u32 s44, s44, 128
	s_addc_u32 s45, s45, 0
	global_load_lds_dwordx4 v220, s[42:43]
	s_mov_b32 m0, s60
	s_nop 0
	global_load_lds_dwordx4 v228, s[42:43]
	s_setprio 1
	v_exp_f32_e32 v80, v80
	v_exp_f32_e32 v81, v81
	v_exp_f32_e32 v82, v82
	v_exp_f32_e32 v83, v83
	v_exp_f32_e32 v84, v84
	v_exp_f32_e32 v85, v85
	v_exp_f32_e32 v86, v86
	v_exp_f32_e32 v87, v87
	v_cvt_pk_fp8_f32 v160, v80, v81
	v_cvt_pk_fp8_f32 v161, v84, v85
	v_exp_f32_e32 v88, v88
	v_exp_f32_e32 v89, v89
	v_cvt_pk_fp8_f32 v160, v82, v83 op_sel:[0,0,1]
	v_cvt_pk_fp8_f32 v161, v86, v87 op_sel:[0,0,1]
	v_exp_f32_e32 v90, v90
	v_exp_f32_e32 v91, v91
	v_exp_f32_e32 v92, v92
	v_exp_f32_e32 v93, v93
	v_exp_f32_e32 v94, v94
	v_exp_f32_e32 v95, v95
	s_waitcnt lgkmcnt(0)
	v_mfma_scale_f32_32x32x64_f8f6f4 v[112:127], v[112:119], v[152:159], v[64:79], v173, v194 op_sel_hi:[0,0,0]
	s_setprio 0
	ds_read_b128 v[80:83], v224 offset:0
	ds_read_b128 v[212:215], v224 offset:2048
	ds_read_b128 v[84:87], v225 offset:0
	ds_read_b128 v[216:219], v225 offset:2048
	v_cvt_pk_fp8_f32 v162, v88, v89
	v_cvt_pk_fp8_f32 v163, v92, v93
	v_exp_f32_e32 v96, v96
	v_exp_f32_e32 v97, v97
	v_cvt_pk_fp8_f32 v162, v90, v91 op_sel:[0,0,1]
	v_cvt_pk_fp8_f32 v163, v94, v95 op_sel:[0,0,1]
	v_exp_f32_e32 v98, v98
	v_exp_f32_e32 v99, v99
	v_exp_f32_e32 v100, v100
	v_exp_f32_e32 v101, v101
	v_exp_f32_e32 v102, v102
	v_exp_f32_e32 v103, v103
	v_mfma_scale_f32_32x32x64_f8f6f4 v[128:143], v[128:135], v[152:159], v[64:79], v173, v194 op_sel_hi:[0,0,0]
	v_cvt_pk_fp8_f32 v164, v96, v97
	v_cvt_pk_fp8_f32 v165, v100, v101
	v_exp_f32_e32 v104, v104
	v_exp_f32_e32 v105, v105
	v_cvt_pk_fp8_f32 v164, v98, v99 op_sel:[0,0,1]
	v_cvt_pk_fp8_f32 v165, v102, v103 op_sel:[0,0,1]
	v_exp_f32_e32 v106, v106
	v_exp_f32_e32 v107, v107
	v_exp_f32_e32 v108, v108
	v_exp_f32_e32 v109, v109
	v_exp_f32_e32 v110, v110
	v_exp_f32_e32 v111, v111
	v_cvt_pk_fp8_f32 v166, v104, v105
	v_cvt_pk_fp8_f32 v167, v108, v109
	v_cvt_pk_fp8_f32 v166, v106, v107 op_sel:[0,0,1]
	v_cvt_pk_fp8_f32 v167, v110, v111 op_sel:[0,0,1]
	s_setprio 2
	s_waitcnt lgkmcnt(0)
	v_mfma_scale_f32_32x32x64_f8f6f4 v[32:47], v[80:87], v[160:167], v[32:47], v194, v194 op_sel_hi:[0,0,0]
	ds_read_b128 v[80:83], v222 offset:16384
	ds_read_b128 v[96:99], v222 offset:18432
	ds_read_b128 v[84:87], v223 offset:16384
	ds_read_b128 v[100:103], v223 offset:18432
	v_max3_f32 v227, v112, v113, v114
	v_max3_f32 v227, v227, v115, v116
	v_max3_f32 v227, v227, v117, v118
	v_max3_f32 v227, v227, v119, v120
	v_max3_f32 v227, v227, v121, v122
	v_max3_f32 v227, v227, v123, v124
	v_max3_f32 v227, v227, v125, v126
	v_max3_f32 v227, v227, v127, v128
	s_mov_b32 m0, s66
	s_add_u32 s42, s42, 0x2000
	s_addc_u32 s43, s43, 0
	global_load_lds_dwordx4 v221, s[44:45]
	v_mfma_scale_f32_32x32x64_f8f6f4 v[16:31], v[212:219], v[160:167], v[16:31], v194, v194 op_sel_hi:[0,0,0]
	v_max3_f32 v226, v129, v130, v131
	v_max3_f32 v226, v226, v132, v133
	v_max3_f32 v226, v226, v134, v135
	v_max3_f32 v226, v226, v136, v137
	v_max3_f32 v226, v226, v138, v139
	v_max3_f32 v226, v226, v140, v141
	v_max3_f32 v226, v226, v142, v143
	s_mov_b32 m0, s67
	s_nop 0
	global_load_lds_dwordx4 v229, s[44:45]
	v_mfma_scale_f32_16x16x128_f8f6f4 v[48:51], v[144:151], v[160:167], v[48:51], v194, v194 op_sel_hi:[0,0,0]
	s_setprio 0
	v_max_f32_e32 v226, v227, v226
	v_cmp_lt_f32_e32 vcc, s36, v226
	s_cbranch_vccnz .Lat_rare_P13

.Lat_back_P14:
	s_waitcnt vmcnt(0) lgkmcnt(0)
	s_barrier
	ds_read_b128 v[112:115], v222 offset:24576
	ds_read_b128 v[128:131], v222 offset:26624
	ds_read_b128 v[116:119], v223 offset:24576
	ds_read_b128 v[132:135], v223 offset:26624
	s_mov_b32 m0, s61
	s_add_u32 s44, s44, 128
	s_addc_u32 s45, s45, 0
	global_load_lds_dwordx4 v220, s[42:43]
	s_setprio 1
	v_exp_f32_e32 v80, v80
	v_exp_f32_e32 v81, v81
	v_exp_f32_e32 v82, v82
	v_exp_f32_e32 v83, v83
	v_exp_f32_e32 v84, v84
	v_exp_f32_e32 v85, v85
	v_exp_f32_e32 v86, v86
	v_exp_f32_e32 v87, v87
	v_cvt_pk_fp8_f32 v160, v80, v81
	v_cvt_pk_fp8_f32 v161, v84, v85
	v_exp_f32_e32 v88, v88
	v_exp_f32_e32 v89, v89
	v_cvt_pk_fp8_f32 v160, v82, v83 op_sel:[0,0,1]
	v_cvt_pk_fp8_f32 v161, v86, v87 op_sel:[0,0,1]
	v_exp_f32_e32 v90, v90
	v_exp_f32_e32 v91, v91
	v_exp_f32_e32 v92, v92
	v_exp_f32_e32 v93, v93
	v_exp_f32_e32 v94, v94
	v_exp_f32_e32 v95, v95
	s_waitcnt lgkmcnt(0)
	v_mfma_scale_f32_32x32x64_f8f6f4 v[112:127], v[112:119], v[152:159], v[64:79], v173, v194 op_sel_hi:[0,0,0]
	s_setprio 0
	ds_read_b128 v[80:83], v224 offset:16384
	ds_read_b128 v[212:215], v224 offset:18432
	ds_read_b128 v[84:87], v225 offset:16384
	ds_read_b128 v[216:219], v225 offset:18432
	v_cvt_pk_fp8_f32 v162, v88, v89
	v_cvt_pk_fp8_f32 v163, v92, v93
	v_exp_f32_e32 v96, v96
	v_exp_f32_e32 v97, v97
	v_cvt_pk_fp8_f32 v162, v90, v91 op_sel:[0,0,1]
	v_cvt_pk_fp8_f32 v163, v94, v95 op_sel:[0,0,1]
	v_exp_f32_e32 v98, v98
	v_exp_f32_e32 v99, v99
	v_exp_f32_e32 v100, v100
	v_exp_f32_e32 v101, v101
	v_exp_f32_e32 v102, v102
	v_exp_f32_e32 v103, v103
	v_mfma_scale_f32_32x32x64_f8f6f4 v[128:143], v[128:135], v[152:159], v[64:79], v173, v194 op_sel_hi:[0,0,0]
	v_cvt_pk_fp8_f32 v164, v96, v97
	v_cvt_pk_fp8_f32 v165, v100, v101
	v_exp_f32_e32 v104, v104
	v_exp_f32_e32 v105, v105
	v_cvt_pk_fp8_f32 v164, v98, v99 op_sel:[0,0,1]
	v_cvt_pk_fp8_f32 v165, v102, v103 op_sel:[0,0,1]
	v_exp_f32_e32 v106, v106
	v_exp_f32_e32 v107, v107
	v_exp_f32_e32 v108, v108
	v_exp_f32_e32 v109, v109
	v_exp_f32_e32 v110, v110
	v_exp_f32_e32 v111, v111
	v_cvt_pk_fp8_f32 v166, v104, v105
	v_cvt_pk_fp8_f32 v167, v108, v109
	v_cvt_pk_fp8_f32 v166, v106, v107 op_sel:[0,0,1]
	v_cvt_pk_fp8_f32 v167, v110, v111 op_sel:[0,0,1]
	s_setprio 2
	s_waitcnt lgkmcnt(0)
	v_mfma_scale_f32_32x32x64_f8f6f4 v[32:47], v[80:87], v[160:167], v[32:47], v194, v194 op_sel_hi:[0,0,0]
	ds_read_b128 v[80:83], v222 offset:0
	ds_read_b128 v[96:99], v222 offset:2048
	ds_read_b128 v[84:87], v223 offset:0
	ds_read_b128 v[100:103], v223 offset:2048
	v_max3_f32 v227, v112, v113, v114
	v_max3_f32 v227, v227, v115, v116
	v_max3_f32 v227, v227, v117, v118
	v_max3_f32 v227, v227, v119, v120
	v_max3_f32 v227, v227, v121, v122
	v_max3_f32 v227, v227, v123, v124
	v_max3_f32 v227, v227, v125, v126
	v_max3_f32 v227, v227, v127, v128
	s_mov_b32 m0, s64
	s_add_u32 s42, s42, 0x2000
	s_addc_u32 s43, s43, 0
	global_load_lds_dwordx4 v221, s[44:45]
	v_mfma_scale_f32_32x32x64_f8f6f4 v[16:31], v[212:219], v[160:167], v[16:31], v194, v194 op_sel_hi:[0,0,0]
	v_max3_f32 v226, v129, v130, v131
	v_max3_f32 v226, v226, v132, v133
	v_max3_f32 v226, v226, v134, v135
	v_max3_f32 v226, v226, v136, v137
	v_max3_f32 v226, v226, v138, v139
	v_max3_f32 v226, v226, v140, v141
	v_max3_f32 v226, v226, v142, v143
	s_mov_b32 m0, s65
	s_nop 0
	global_load_lds_dwordx4 v229, s[44:45]
	v_mfma_scale_f32_16x16x128_f8f6f4 v[48:51], v[144:151], v[160:167], v[48:51], v194, v194 op_sel_hi:[0,0,0]
	s_setprio 0
	v_max_f32_e32 v226, v227, v226
	v_cmp_lt_f32_e32 vcc, s36, v226
	s_cbranch_vccnz .Lat_rare_P15

.Lat_back_P16:
	s_waitcnt vmcnt(0) lgkmcnt(0)
	s_barrier
	ds_read_b128 v[112:115], v222 offset:8192
	ds_read_b128 v[128:131], v222 offset:10240
	ds_read_b128 v[116:119], v223 offset:8192
	ds_read_b128 v[132:135], v223 offset:10240
	s_setprio 1
	v_exp_f32_e32 v80, v80
	v_exp_f32_e32 v81, v81
	v_exp_f32_e32 v82, v82
	v_exp_f32_e32 v83, v83
	v_exp_f32_e32 v84, v84
	v_exp_f32_e32 v85, v85
	v_exp_f32_e32 v86, v86
	v_exp_f32_e32 v87, v87
	v_cvt_pk_fp8_f32 v160, v80, v81
	v_cvt_pk_fp8_f32 v161, v84, v85
	v_exp_f32_e32 v88, v88
	v_exp_f32_e32 v89, v89
	v_cvt_pk_fp8_f32 v160, v82, v83 op_sel:[0,0,1]
	v_cvt_pk_fp8_f32 v161, v86, v87 op_sel:[0,0,1]
	v_exp_f32_e32 v90, v90
	v_exp_f32_e32 v91, v91
	v_exp_f32_e32 v92, v92
	v_exp_f32_e32 v93, v93
	v_exp_f32_e32 v94, v94
	v_exp_f32_e32 v95, v95
	s_waitcnt lgkmcnt(0)
	v_mfma_scale_f32_32x32x64_f8f6f4 v[112:127], v[112:119], v[152:159], v[64:79], v173, v194 op_sel_hi:[0,0,0]
	s_setprio 0
	ds_read_b128 v[80:83], v224 offset:0
	ds_read_b128 v[136:139], v224 offset:2048
	ds_read_b128 v[84:87], v225 offset:0
	ds_read_b128 v[140:143], v225 offset:2048
	v_cvt_pk_fp8_f32 v162, v88, v89
	v_cvt_pk_fp8_f32 v163, v92, v93
	v_exp_f32_e32 v96, v96
	v_exp_f32_e32 v97, v97
	v_cvt_pk_fp8_f32 v162, v90, v91 op_sel:[0,0,1]
	v_cvt_pk_fp8_f32 v163, v94, v95 op_sel:[0,0,1]
	v_exp_f32_e32 v98, v98
	v_exp_f32_e32 v99, v99
	v_exp_f32_e32 v100, v100
	v_exp_f32_e32 v101, v101
	v_exp_f32_e32 v102, v102
	v_exp_f32_e32 v103, v103
	v_mfma_scale_f32_32x32x64_f8f6f4 v[64:79], v[128:135], v[152:159], v[64:79], v173, v194 op_sel_hi:[0,0,0]
	v_cvt_pk_fp8_f32 v164, v96, v97
	v_cvt_pk_fp8_f32 v165, v100, v101
	v_exp_f32_e32 v104, v104
	v_exp_f32_e32 v105, v105
	v_cvt_pk_fp8_f32 v164, v98, v99 op_sel:[0,0,1]
	v_cvt_pk_fp8_f32 v165, v102, v103 op_sel:[0,0,1]
	v_exp_f32_e32 v106, v106
	v_exp_f32_e32 v107, v107
	v_exp_f32_e32 v108, v108
	v_exp_f32_e32 v109, v109
	v_exp_f32_e32 v110, v110
	v_exp_f32_e32 v111, v111
	v_cvt_pk_fp8_f32 v166, v104, v105
	v_cvt_pk_fp8_f32 v167, v108, v109
	v_cvt_pk_fp8_f32 v166, v106, v107 op_sel:[0,0,1]
	v_cvt_pk_fp8_f32 v167, v110, v111 op_sel:[0,0,1]
	s_setprio 2
	s_waitcnt lgkmcnt(0)
	v_mfma_scale_f32_32x32x64_f8f6f4 v[32:47], v[80:87], v[160:167], v[32:47], v194, v194 op_sel_hi:[0,0,0]
	v_max3_f32 v227, v112, v113, v114
	v_max3_f32 v227, v227, v115, v116
	v_max3_f32 v227, v227, v117, v118
	v_max3_f32 v227, v227, v119, v120
	v_max3_f32 v227, v227, v121, v122
	v_max3_f32 v227, v227, v123, v124
	v_max3_f32 v227, v227, v125, v126
	v_max3_f32 v227, v227, v127, v64
	v_mfma_scale_f32_32x32x64_f8f6f4 v[16:31], v[136:143], v[160:167], v[16:31], v194, v194 op_sel_hi:[0,0,0]
	v_max3_f32 v226, v65, v66, v67
	v_max3_f32 v226, v226, v68, v69
	v_max3_f32 v226, v226, v70, v71
	v_max3_f32 v226, v226, v72, v73
	v_max3_f32 v226, v226, v74, v75
	v_max3_f32 v226, v226, v76, v77
	v_max3_f32 v226, v226, v78, v79
	v_mfma_scale_f32_16x16x128_f8f6f4 v[48:51], v[144:151], v[160:167], v[48:51], v194, v194 op_sel_hi:[0,0,0]
	s_setprio 0
	v_max_f32_e32 v226, v227, v226
	v_cmp_lt_f32_e32 vcc, s36, v226
	s_cbranch_vccnz .Lat_rare_P17
